# tail converters throttled to 4 waves per workgroup so HBM is not saturated while the last GEMM round runs
# baseline (speedup 1.0000x reference)
; #define LAS __attribute__((address_space(3)))
; __global__ void __launch_bounds__(NWAVES * 64, 2) mk_fwd(Args args) {
;     ...
;             PH_LOCALS
;             LAS float* scr = (LAS float*)(lds + RING_OFF + wave * 16640);   static_assert(8 * 16640 <= LDSCTL_OFF, "converter scratch below the LDS control words");
;             constexpr int I_UP = (D / 64) * (NUP / 64), I_DN = (DFF / 64) * (D / 64), I_IN = (D / 64) * (DINP / 64), I_GLU = 16 * 16, I_L = 4 * 16, I_V1 = 16 * 4, I_V2 = 4 * 16,
;                           I_BS5 = 16 * 32, I_BAT = 8 * 32, I_BRW = 16 * 32, I_OUT = 32 * 32;
;             constexpr int NITEMS = 2 * I_UP + 2 * I_DN + I_IN + I_GLU + 3 * I_L + I_V1 + I_V2 + I_BS5 + I_BAT + I_BRW + I_OUT;
;             const int lv = l > 0 ? l - 1 : 0;
;     ...
;             for (int it = gw; it < NITEMS; it += NGW) {
;                 ConvItem ca; CONV_DESC(ca, it);
;                 float va[64];
;                 conv_load(ca, lane, va);
;                 conv_store(ca, scr, lane, va);
;             }
.LBB0_142:
	v_readlane_b32 s99, v254, 35
	v_readlane_b32 s98, v254, 38
	s_nop 3
	s_cmp_lt_u32 s99, 96
	s_cbranch_scc1 .Lcvskip_p1
	v_mov_b32_e32 v250, v254
	v_mov_b32_e32 v251, v255
	v_writelane_b32 v252, s0, 0
	s_nop 0
	v_writelane_b32 v252, s1, 1
	s_nop 0
	v_writelane_b32 v252, s2, 2
	s_nop 0
	v_writelane_b32 v252, s3, 3
	s_nop 0
	v_writelane_b32 v252, s4, 4
	s_nop 0
	v_writelane_b32 v252, s5, 5
	s_nop 0
	v_writelane_b32 v252, s6, 6
	s_nop 0
	v_writelane_b32 v252, s7, 7
	s_nop 0
	v_writelane_b32 v252, s8, 8
	s_nop 0
	v_writelane_b32 v252, s9, 9
	s_nop 0
	v_writelane_b32 v252, s10, 10
	s_nop 0
	v_writelane_b32 v252, s11, 11
	s_nop 0
	v_writelane_b32 v252, s12, 12
	s_nop 0
	v_writelane_b32 v252, s13, 13
	s_nop 0
	v_writelane_b32 v252, s14, 14
	s_nop 0
	v_writelane_b32 v252, s15, 15
	s_nop 0
	v_writelane_b32 v252, s16, 16
	s_nop 0
	v_writelane_b32 v252, s17, 17
	s_nop 0
	v_writelane_b32 v252, s18, 18
	s_nop 0
	v_writelane_b32 v252, s19, 19
	s_nop 0
	v_writelane_b32 v252, s20, 20
	s_nop 0
	v_writelane_b32 v252, s21, 21
	s_nop 0
	v_writelane_b32 v252, s22, 22
	s_nop 0
	v_writelane_b32 v252, s23, 23
	s_nop 0
	v_writelane_b32 v252, s24, 24
	s_nop 0
	v_writelane_b32 v252, s25, 25
	s_nop 0
	v_writelane_b32 v252, s26, 26
	s_nop 0
	v_writelane_b32 v252, s27, 27
	s_nop 0
	v_writelane_b32 v252, s28, 28
	s_nop 0
	v_writelane_b32 v252, s29, 29
	s_nop 0
	v_writelane_b32 v252, s30, 30
	s_nop 0
	v_writelane_b32 v252, s31, 31
	s_nop 0
	v_writelane_b32 v252, s32, 32
	s_nop 0
	v_writelane_b32 v252, s33, 33
	s_nop 0
	v_writelane_b32 v252, s34, 34
	s_nop 0
	v_writelane_b32 v252, s35, 35
	s_nop 0
	v_writelane_b32 v252, s36, 36
	s_nop 0
	v_writelane_b32 v252, s37, 37
	s_nop 0
	v_writelane_b32 v252, s38, 38
	s_nop 0
	v_writelane_b32 v252, s39, 39
	s_nop 0
	v_writelane_b32 v252, s40, 40
	s_nop 0
	v_writelane_b32 v252, s41, 41
	s_nop 0
	v_writelane_b32 v252, s42, 42
	s_nop 0
	v_writelane_b32 v252, s43, 43
	s_nop 0
	v_writelane_b32 v252, s44, 44
	s_nop 0
	v_writelane_b32 v252, s45, 45
	s_nop 0
	v_writelane_b32 v252, s46, 46
	s_nop 0
	v_writelane_b32 v252, s47, 47
	s_nop 0
	v_writelane_b32 v252, s48, 48
	s_nop 0
	v_writelane_b32 v252, s49, 49
	s_nop 0
	v_writelane_b32 v252, s50, 50
	s_nop 0
	v_writelane_b32 v252, s51, 51
	s_nop 0
	v_writelane_b32 v252, s52, 52
	s_nop 0
	v_writelane_b32 v252, s53, 53
	s_nop 0
	v_writelane_b32 v252, s54, 54
	s_nop 0
	v_writelane_b32 v252, s55, 55
	s_nop 0
	v_writelane_b32 v252, s56, 56
	s_nop 0
	v_writelane_b32 v252, s57, 57
	s_nop 0
	v_writelane_b32 v252, s58, 58
	s_nop 0
	v_writelane_b32 v252, s59, 59
	s_nop 0
	v_writelane_b32 v252, s60, 60
	s_nop 0
	v_writelane_b32 v252, s61, 61
	s_nop 0
	v_writelane_b32 v252, s62, 62
	s_nop 0
	v_writelane_b32 v252, s63, 63
	s_nop 0
	v_writelane_b32 v253, s64, 0
	s_nop 0
	v_writelane_b32 v253, s65, 1
	s_nop 0
	v_writelane_b32 v253, s66, 2
	s_nop 0
	v_writelane_b32 v253, s67, 3
	s_nop 0
	v_writelane_b32 v253, s68, 4
	s_nop 0
	v_writelane_b32 v253, s69, 5
	s_nop 0
	v_writelane_b32 v253, s70, 6
	s_nop 0
	v_writelane_b32 v253, s71, 7
	s_nop 0
	v_writelane_b32 v253, s72, 8
	s_nop 0
	v_writelane_b32 v253, s73, 9
	s_nop 0
	v_writelane_b32 v253, s74, 10
	s_nop 0
	v_writelane_b32 v253, s75, 11
	s_nop 0
	v_writelane_b32 v253, s76, 12
	s_nop 0
	v_writelane_b32 v253, s77, 13
	s_nop 0
	v_writelane_b32 v253, s78, 14
	s_nop 0
	v_writelane_b32 v253, s79, 15
	s_nop 0
	v_writelane_b32 v253, s80, 16
	s_nop 0
	v_writelane_b32 v253, s81, 17
	s_nop 0
	v_writelane_b32 v253, s82, 18
	s_nop 0
	v_writelane_b32 v253, s83, 19
	s_nop 0
	v_writelane_b32 v253, s84, 20
	s_nop 0
	v_writelane_b32 v253, s85, 21
	s_nop 0
	v_writelane_b32 v253, s86, 22
	s_nop 0
	v_writelane_b32 v253, s87, 23
	s_nop 0
	v_writelane_b32 v253, s88, 24
	s_nop 0
	v_writelane_b32 v253, s89, 25
	s_nop 0
	v_writelane_b32 v253, s90, 26
	s_nop 0
	v_writelane_b32 v253, s91, 27
	s_nop 0
	v_writelane_b32 v253, s92, 28
	s_nop 0
	v_writelane_b32 v253, s93, 29
	s_nop 0
	v_writelane_b32 v253, s94, 30
	s_nop 0
	v_writelane_b32 v253, s95, 31
	s_nop 0
	v_writelane_b32 v253, s96, 32
	s_nop 0
	v_writelane_b32 v253, s97, 33
	s_nop 0
	v_writelane_b32 v253, vcc_lo, 34
	s_nop 0
	v_writelane_b32 v253, vcc_hi, 35
	s_nop 1
	v_readlane_b32 s84, v254, 35
	s_nop 3
	v_readlane_b32 s0, v254, 8
	v_readlane_b32 s4, v254, 10
	v_readlane_b32 s1, v254, 9
	v_mbcnt_lo_u32_b32 v11, -1, 0
	v_mbcnt_hi_u32_b32 v11, -1, v11
	s_load_dword s6, s[0:1], 0x0
	s_mov_b32 s3, s84
	s_waitcnt lgkmcnt(0)
	s_movk_i32 s6, 80
	s_cmp_gt_u32 s4, 3
	s_cbranch_scc1 .Lcvp10_ret
; #define LAS __attribute__((address_space(3)))
; __global__ void __launch_bounds__(NWAVES * 64, 2) mk_fwd(Args args) {
;     ...
;             PH_LOCALS
;             LAS float* scr = (LAS float*)(lds + RING_OFF + wave * 16640);   static_assert(8 * 16640 <= LDSCTL_OFF, "converter scratch below the LDS control words");
;             constexpr int I_UP = (D / 64) * (NUP / 64), I_DN = (DFF / 64) * (D / 64), I_IN = (D / 64) * (DINP / 64), I_GLU = 16 * 16, I_L = 4 * 16, I_V1 = 16 * 4, I_V2 = 4 * 16,
;                           I_BS5 = 16 * 32, I_BAT = 8 * 32, I_BRW = 16 * 32, I_OUT = 32 * 32;
;             constexpr int NITEMS = 2 * I_UP + 2 * I_DN + I_IN + I_GLU + 3 * I_L + I_V1 + I_V2 + I_BS5 + I_BAT + I_BRW + I_OUT;
;             const int lv = l > 0 ? l - 1 : 0;
;     ...
;             for (int it = gw; it < NITEMS; it += NGW) {
;                 ConvItem ca; CONV_DESC(ca, it);
;                 float va[64];
;                 conv_load(ca, lane, va);
;                 conv_store(ca, scr, lane, va);
;             }
	s_lshl_b32 s3, s3, 2
	v_readlane_b32 s0, v254, 0
	s_add_i32 s3, s3, s4
	s_add_i32 s3, s3, 0x1400
	v_readlane_b32 s1, v254, 1
	s_cmpk_gt_i32 s3, 11007
	s_cbranch_scc1 .Lcvp10_ret
	s_load_dwordx2 s[8:9], s[0:1], 0x138
	v_readlane_b32 s14, v254, 38
	s_mulk_i32 s4, 0x4100
	s_add_i32 s7, s4, 0
	v_sub_u32_e64 v0, s14, 1 clamp
	s_lshl_b32 s33, s6, 3
	v_readfirstlane_b32 s4, v0
	s_lshl_b32 s96, s4, 16
	s_waitcnt lgkmcnt(0)
	s_add_u32 s4, s8, 0x22800000
	s_addc_u32 s5, s9, 0
	v_writelane_b32 v254, s4, 39
	s_mov_b32 s15, s97
	v_and_b32_e32 v0, 7, v11
	v_writelane_b32 v254, s5, 40
	s_add_u32 s4, s8, 0x22780000
	s_addc_u32 s5, s9, 0
	v_writelane_b32 v254, s4, 41
	v_ashrrev_i32_e32 v13, 3, v11
	v_lshlrev_b32_e32 v10, 3, v0
	v_writelane_b32 v254, s5, 42
	s_lshl_b32 s4, s14, 18
	s_add_u32 s10, s8, 0x22700000
	s_addc_u32 s11, s9, 0
	v_writelane_b32 v254, s10, 43
	s_mov_b32 s5, s97
	v_mul_u32_u24_e32 v0, 0x820, v0
	v_writelane_b32 v254, s11, 44
	s_mul_i32 s10, s14, 0x18000
	s_mov_b32 s11, s97
	v_writelane_b32 v254, s10, 45
	v_lshlrev_b32_e32 v1, 2, v13
	v_lshl_add_u32 v12, v11, 2, s7
	v_writelane_b32 v254, s11, 46
	s_add_u32 s10, s8, 0x22680000
	s_addc_u32 s11, s9, 0
	v_writelane_b32 v254, s10, 47
	v_add3_u32 v14, s7, v0, v1
	s_mov_b32 s41, s97
	v_writelane_b32 v254, s11, 48
	s_add_u32 s10, s8, 0x22600000
	s_addc_u32 s11, s9, 0
	v_writelane_b32 v254, s10, 49
	s_nop 1
	v_writelane_b32 v254, s11, 50
	s_lshl_b32 s10, s14, 20
	s_mov_b32 s11, s97
	v_writelane_b32 v254, s10, 51
	s_nop 1
	v_writelane_b32 v254, s11, 52
	s_add_u32 s10, s8, 0x22400000
	s_addc_u32 s11, s9, 0
	v_writelane_b32 v254, s10, 53
	s_nop 1
	v_writelane_b32 v254, s11, 54
	s_lshl_b32 s10, s14, 21
	s_mov_b32 s11, s97
	v_writelane_b32 v254, s10, 55
	s_nop 1
	v_writelane_b32 v254, s11, 56
	s_add_u32 s10, s8, 0x22e80000
	s_addc_u32 s11, s9, 0
	v_writelane_b32 v254, s10, 57
	s_nop 1
	v_writelane_b32 v254, s11, 58
	s_add_u32 s10, s8, 0x27b80000
	s_addc_u32 s11, s9, 0
	v_writelane_b32 v254, s10, 59
	s_nop 1
	v_writelane_b32 v254, s11, 60
	s_add_u32 s10, s8, 0x22880000
	s_addc_u32 s11, s9, 0
	v_writelane_b32 v254, s10, 61
	s_nop 1
	v_writelane_b32 v254, s11, 62
	s_lshl_b32 s10, s14, 22
	s_add_u32 s12, s8, 0x23280000
	s_addc_u32 s13, s9, 0
	v_writelane_b32 v254, s12, 63
	s_mov_b32 s11, s97
	s_nop 0
	v_writelane_b32 v255, s13, 0
	s_mul_i32 s12, s14, 0xac0000
	s_mov_b32 s13, s97
	v_writelane_b32 v255, s12, 1
	s_nop 1
	v_writelane_b32 v255, s13, 2
	s_add_u32 s12, s8, 0x26580000
	s_addc_u32 s13, s9, 0
	v_writelane_b32 v255, s12, 3
	s_nop 1
	v_writelane_b32 v255, s13, 4
	s_add_u32 s12, s8, 0x1d200000
	s_addc_u32 s13, s9, 0
	s_lshl_b32 s40, s14, 11
	v_writelane_b32 v255, s12, 5
	s_add_u32 s16, s8, 0x1e800000
	s_addc_u32 s17, s9, 0
	v_writelane_b32 v255, s13, 6
	v_writelane_b32 v255, s16, 7
	s_mul_i32 s12, s14, 0x1de0000
	s_mul_i32 s14, s14, 0x1580000
	v_writelane_b32 v255, s17, 8
	v_writelane_b32 v255, s14, 9
	s_mov_b32 s13, s97
	s_nop 0
	v_writelane_b32 v255, s15, 10
	s_add_u32 s14, s8, 0x23a80000
	s_addc_u32 s15, s9, 0
	v_writelane_b32 v255, s14, 11
	s_add_u32 s8, s8, 0x1a700000
	s_addc_u32 s9, s9, 0
	v_writelane_b32 v255, s15, 12
	v_writelane_b32 v255, s8, 13
	s_lshl_b64 s[4:5], s[4:5], 2
	s_lshl_b32 s7, s3, 4
	v_writelane_b32 v255, s9, 14
	v_writelane_b32 v255, s4, 15
	s_add_i32 s72, s7, 0xc00
	s_lshl_b32 s7, s3, 1
	v_writelane_b32 v255, s5, 16
	s_lshl_b64 s[4:5], s[10:11], 2
	v_writelane_b32 v255, s4, 17
	s_lshl_b32 s66, s3, 6
	s_lshl_b32 s67, s6, 9
	v_writelane_b32 v255, s5, 18
	s_lshl_b64 s[4:5], s[12:13], 2
	v_writelane_b32 v255, s4, 19
	s_lshl_b32 s68, s3, 5
	s_lshl_b32 s69, s6, 8
	v_writelane_b32 v255, s5, 20
	v_writelane_b32 v255, s80, 21
	s_lshl_b32 s70, s3, 2
	s_lshl_b32 s71, s6, 5
	v_writelane_b32 v255, s81, 22
	v_writelane_b32 v255, s82, 23
	s_lshl_b32 s73, s6, 7
	s_add_i32 s74, s7, 0x13500
	s_lshl_b32 s75, s6, 4
	v_writelane_b32 v255, s83, 24
	s_branch .Lcvp10_31

; #define LAS __attribute__((address_space(3)))
; __global__ void __launch_bounds__(NWAVES * 64, 2) mk_fwd(Args args) {
;     ...
;             PH_LOCALS
;             LAS float* scr = (LAS float*)(lds + RING_OFF + wave * 16640);   static_assert(8 * 16640 <= LDSCTL_OFF, "converter scratch below the LDS control words");
;             constexpr int I_UP = (D / 64) * (NUP / 64), I_DN = (DFF / 64) * (D / 64), I_IN = (D / 64) * (DINP / 64), I_GLU = 16 * 16, I_L = 4 * 16, I_V1 = 16 * 4, I_V2 = 4 * 16,
;                           I_BS5 = 16 * 32, I_BAT = 8 * 32, I_BRW = 16 * 32, I_OUT = 32 * 32;
;             constexpr int NITEMS = 2 * I_UP + 2 * I_DN + I_IN + I_GLU + 3 * I_L + I_V1 + I_V2 + I_BS5 + I_BAT + I_BRW + I_OUT;
;             const int lv = l > 0 ? l - 1 : 0;
;     ...
;             for (int it = gw; it < NITEMS; it += NGW) {
;                 ConvItem ca; CONV_DESC(ca, it);
;                 float va[64];
;                 conv_load(ca, lane, va);
;                 conv_store(ca, scr, lane, va);
;             }
.Lcvp10_ret:
.Lcvrs_p10:
	v_readlane_b32 s0, v254, 8
	v_readlane_b32 s4, v254, 10
	v_readlane_b32 s1, v254, 9
	v_mbcnt_lo_u32_b32 v11, -1, 0
	v_mbcnt_hi_u32_b32 v11, -1, v11
	s_load_dword s6, s[0:1], 0x0
	s_mov_b32 s3, s84
	s_waitcnt lgkmcnt(0)
	s_movk_i32 s6, 80
	s_cmp_gt_u32 s4, 3
	s_cbranch_scc1 .Lcvp11_ret
	s_lshl_b32 s3, s3, 2
	v_readlane_b32 s0, v254, 0
	s_add_i32 s3, s3, s4
	s_add_i32 s3, s3, 0x6100
	v_readlane_b32 s1, v254, 1
	s_cmpk_gt_i32 s3, 26495
	s_cbranch_scc1 .Lcvp11_ret
	s_load_dwordx2 s[8:9], s[0:1], 0x138
	v_readlane_b32 s14, v254, 38
	s_mulk_i32 s4, 0x4100
	s_add_i32 s7, s4, 0
	v_sub_u32_e64 v0, s14, 1 clamp
	s_lshl_b32 s33, s6, 3
	v_readfirstlane_b32 s4, v0
	s_lshl_b32 s96, s4, 16
	s_waitcnt lgkmcnt(0)
	s_add_u32 s4, s8, 0x22800000
	s_addc_u32 s5, s9, 0
	v_writelane_b32 v254, s4, 39
	s_mov_b32 s15, s97
	v_and_b32_e32 v0, 7, v11
	v_writelane_b32 v254, s5, 40
	s_add_u32 s4, s8, 0x22780000
	s_addc_u32 s5, s9, 0
	v_writelane_b32 v254, s4, 41
	v_ashrrev_i32_e32 v13, 3, v11
	v_lshlrev_b32_e32 v10, 3, v0
	v_writelane_b32 v254, s5, 42
	s_lshl_b32 s4, s14, 18
	s_add_u32 s10, s8, 0x22700000
	s_addc_u32 s11, s9, 0
	v_writelane_b32 v254, s10, 43
	s_mov_b32 s5, s97
	v_mul_u32_u24_e32 v0, 0x820, v0
	v_writelane_b32 v254, s11, 44
	s_mul_i32 s10, s14, 0x18000
	s_mov_b32 s11, s97
	v_writelane_b32 v254, s10, 45
	v_lshlrev_b32_e32 v1, 2, v13
	v_lshl_add_u32 v12, v11, 2, s7
	v_writelane_b32 v254, s11, 46
	s_add_u32 s10, s8, 0x22680000
	s_addc_u32 s11, s9, 0
	v_writelane_b32 v254, s10, 47
	v_add3_u32 v14, s7, v0, v1
	s_mov_b32 s41, s97
	v_writelane_b32 v254, s11, 48
	s_add_u32 s10, s8, 0x22600000
	s_addc_u32 s11, s9, 0
	v_writelane_b32 v254, s10, 49
	s_nop 1
	v_writelane_b32 v254, s11, 50
	s_lshl_b32 s10, s14, 20
	s_mov_b32 s11, s97
	v_writelane_b32 v254, s10, 51
	s_nop 1
	v_writelane_b32 v254, s11, 52
	s_add_u32 s10, s8, 0x22400000
	s_addc_u32 s11, s9, 0
	v_writelane_b32 v254, s10, 53
	s_nop 1
	v_writelane_b32 v254, s11, 54
	s_lshl_b32 s10, s14, 21
	s_mov_b32 s11, s97
	v_writelane_b32 v254, s10, 55
	s_nop 1
	v_writelane_b32 v254, s11, 56
	s_add_u32 s10, s8, 0x22e80000
	s_addc_u32 s11, s9, 0
	v_writelane_b32 v254, s10, 57
	s_nop 1
	v_writelane_b32 v254, s11, 58
	s_add_u32 s10, s8, 0x27b80000
	s_addc_u32 s11, s9, 0
	v_writelane_b32 v254, s10, 59
	s_nop 1
	v_writelane_b32 v254, s11, 60
	s_add_u32 s10, s8, 0x22880000
	s_addc_u32 s11, s9, 0
	v_writelane_b32 v254, s10, 61
	s_nop 1
	v_writelane_b32 v254, s11, 62
	s_lshl_b32 s10, s14, 22
	s_add_u32 s12, s8, 0x23280000
	s_addc_u32 s13, s9, 0
	v_writelane_b32 v254, s12, 63
	s_mov_b32 s11, s97
	s_nop 0
	v_writelane_b32 v255, s13, 0
	s_mul_i32 s12, s14, 0xac0000
	s_mov_b32 s13, s97
	v_writelane_b32 v255, s12, 1
	s_nop 1
	v_writelane_b32 v255, s13, 2
	s_add_u32 s12, s8, 0x26580000
	s_addc_u32 s13, s9, 0
	v_writelane_b32 v255, s12, 3
	s_nop 1
	v_writelane_b32 v255, s13, 4
	s_add_u32 s12, s8, 0x1d200000
	s_addc_u32 s13, s9, 0
	s_lshl_b32 s40, s14, 11
	v_writelane_b32 v255, s12, 5
	s_add_u32 s16, s8, 0x1e800000
	s_addc_u32 s17, s9, 0
	v_writelane_b32 v255, s13, 6
	v_writelane_b32 v255, s16, 7
	s_mul_i32 s12, s14, 0x1de0000
	s_mul_i32 s14, s14, 0x1580000
	v_writelane_b32 v255, s17, 8
	v_writelane_b32 v255, s14, 9
	s_mov_b32 s13, s97
	s_nop 0
	v_writelane_b32 v255, s15, 10
	s_add_u32 s14, s8, 0x23a80000
	s_addc_u32 s15, s9, 0
	v_writelane_b32 v255, s14, 11
	s_add_u32 s8, s8, 0x1a700000
	s_addc_u32 s9, s9, 0
	v_writelane_b32 v255, s15, 12
	v_writelane_b32 v255, s8, 13
	s_lshl_b64 s[4:5], s[4:5], 2
	s_lshl_b32 s7, s3, 4
	v_writelane_b32 v255, s9, 14
	v_writelane_b32 v255, s4, 15
	s_add_i32 s72, s7, 0xc00
	s_lshl_b32 s7, s3, 1
	v_writelane_b32 v255, s5, 16
	s_lshl_b64 s[4:5], s[10:11], 2
	v_writelane_b32 v255, s4, 17
	s_lshl_b32 s66, s3, 6
	s_lshl_b32 s67, s6, 9
	v_writelane_b32 v255, s5, 18
	s_lshl_b64 s[4:5], s[12:13], 2
	v_writelane_b32 v255, s4, 19
	s_lshl_b32 s68, s3, 5
	s_lshl_b32 s69, s6, 8
	v_writelane_b32 v255, s5, 20
	v_writelane_b32 v255, s80, 21
	s_lshl_b32 s70, s3, 2
	s_lshl_b32 s71, s6, 5
	v_writelane_b32 v255, s81, 22
	v_writelane_b32 v255, s82, 23
	s_lshl_b32 s73, s6, 7
	s_add_i32 s74, s7, 0x13500
	s_lshl_b32 s75, s6, 4
	v_writelane_b32 v255, s83, 24
	s_branch .Lcvp11_31

; #define LAS __attribute__((address_space(3)))
; #define IN(k) in_range(lo, hi, (k))
; __global__ void __launch_bounds__(NWAVES * 64, 2) mk_fwd(Args args) {
;     ...
;         if (EN(0) && IN(pb + 0)) {
;             PH_LOCALS
;             LAS float* scr = (LAS float*)(lds + RING_OFF + wave * 16640);   static_assert(8 * 16640 <= LDSCTL_OFF, "converter scratch below the LDS control words");
;             constexpr int I_UP = (D / 64) * (NUP / 64), I_DN = (DFF / 64) * (D / 64), I_IN = (D / 64) * (DINP / 64), I_GLU = 16 * 16, I_L = 4 * 16, I_V1 = 16 * 4, I_V2 = 4 * 16,
;                           I_BS5 = 16 * 32, I_BAT = 8 * 32, I_BRW = 16 * 32, I_OUT = 32 * 32;
;             constexpr int NITEMS = 2 * I_UP + 2 * I_DN + I_IN + I_GLU + 3 * I_L + I_V1 + I_V2 + I_BS5 + I_BAT + I_BRW + I_OUT;
;             const int lv = l > 0 ? l - 1 : 0;
.LBB0_346:
	v_readlane_b32 s99, v254, 35
	v_readlane_b32 s98, v254, 38
	s_nop 3
	s_cmp_lt_u32 s99, 128
	s_cbranch_scc1 .Lcvskip_p3
	v_mov_b32_e32 v250, v254
	v_mov_b32_e32 v251, v255
	v_writelane_b32 v252, s0, 0
	s_nop 0
	v_writelane_b32 v252, s1, 1
	s_nop 0
	v_writelane_b32 v252, s2, 2
	s_nop 0
	v_writelane_b32 v252, s3, 3
	s_nop 0
	v_writelane_b32 v252, s4, 4
	s_nop 0
	v_writelane_b32 v252, s5, 5
	s_nop 0
	v_writelane_b32 v252, s6, 6
	s_nop 0
	v_writelane_b32 v252, s7, 7
	s_nop 0
	v_writelane_b32 v252, s8, 8
	s_nop 0
	v_writelane_b32 v252, s9, 9
	s_nop 0
	v_writelane_b32 v252, s10, 10
	s_nop 0
	v_writelane_b32 v252, s11, 11
	s_nop 0
	v_writelane_b32 v252, s12, 12
	s_nop 0
	v_writelane_b32 v252, s13, 13
	s_nop 0
	v_writelane_b32 v252, s14, 14
	s_nop 0
	v_writelane_b32 v252, s15, 15
	s_nop 0
	v_writelane_b32 v252, s16, 16
	s_nop 0
	v_writelane_b32 v252, s17, 17
	s_nop 0
	v_writelane_b32 v252, s18, 18
	s_nop 0
	v_writelane_b32 v252, s19, 19
	s_nop 0
	v_writelane_b32 v252, s20, 20
	s_nop 0
	v_writelane_b32 v252, s21, 21
	s_nop 0
	v_writelane_b32 v252, s22, 22
	s_nop 0
	v_writelane_b32 v252, s23, 23
	s_nop 0
	v_writelane_b32 v252, s24, 24
	s_nop 0
	v_writelane_b32 v252, s25, 25
	s_nop 0
	v_writelane_b32 v252, s26, 26
	s_nop 0
	v_writelane_b32 v252, s27, 27
	s_nop 0
	v_writelane_b32 v252, s28, 28
	s_nop 0
	v_writelane_b32 v252, s29, 29
	s_nop 0
	v_writelane_b32 v252, s30, 30
	s_nop 0
	v_writelane_b32 v252, s31, 31
	s_nop 0
	v_writelane_b32 v252, s32, 32
	s_nop 0
	v_writelane_b32 v252, s33, 33
	s_nop 0
	v_writelane_b32 v252, s34, 34
	s_nop 0
	v_writelane_b32 v252, s35, 35
	s_nop 0
	v_writelane_b32 v252, s36, 36
	s_nop 0
	v_writelane_b32 v252, s37, 37
	s_nop 0
	v_writelane_b32 v252, s38, 38
	s_nop 0
	v_writelane_b32 v252, s39, 39
	s_nop 0
	v_writelane_b32 v252, s40, 40
	s_nop 0
	v_writelane_b32 v252, s41, 41
	s_nop 0
	v_writelane_b32 v252, s42, 42
	s_nop 0
	v_writelane_b32 v252, s43, 43
	s_nop 0
	v_writelane_b32 v252, s44, 44
	s_nop 0
	v_writelane_b32 v252, s45, 45
	s_nop 0
	v_writelane_b32 v252, s46, 46
	s_nop 0
	v_writelane_b32 v252, s47, 47
	s_nop 0
	v_writelane_b32 v252, s48, 48
	s_nop 0
	v_writelane_b32 v252, s49, 49
	s_nop 0
	v_writelane_b32 v252, s50, 50
	s_nop 0
	v_writelane_b32 v252, s51, 51
	s_nop 0
	v_writelane_b32 v252, s52, 52
	s_nop 0
	v_writelane_b32 v252, s53, 53
	s_nop 0
	v_writelane_b32 v252, s54, 54
	s_nop 0
	v_writelane_b32 v252, s55, 55
	s_nop 0
	v_writelane_b32 v252, s56, 56
	s_nop 0
	v_writelane_b32 v252, s57, 57
	s_nop 0
	v_writelane_b32 v252, s58, 58
	s_nop 0
	v_writelane_b32 v252, s59, 59
	s_nop 0
	v_writelane_b32 v252, s60, 60
	s_nop 0
	v_writelane_b32 v252, s61, 61
	s_nop 0
	v_writelane_b32 v252, s62, 62
	s_nop 0
	v_writelane_b32 v252, s63, 63
	s_nop 0
	v_writelane_b32 v253, s64, 0
	s_nop 0
	v_writelane_b32 v253, s65, 1
	s_nop 0
	v_writelane_b32 v253, s66, 2
	s_nop 0
	v_writelane_b32 v253, s67, 3
	s_nop 0
	v_writelane_b32 v253, s68, 4
	s_nop 0
	v_writelane_b32 v253, s69, 5
	s_nop 0
	v_writelane_b32 v253, s70, 6
	s_nop 0
	v_writelane_b32 v253, s71, 7
	s_nop 0
	v_writelane_b32 v253, s72, 8
	s_nop 0
	v_writelane_b32 v253, s73, 9
	s_nop 0
	v_writelane_b32 v253, s74, 10
	s_nop 0
	v_writelane_b32 v253, s75, 11
	s_nop 0
	v_writelane_b32 v253, s76, 12
	s_nop 0
	v_writelane_b32 v253, s77, 13
	s_nop 0
	v_writelane_b32 v253, s78, 14
	s_nop 0
	v_writelane_b32 v253, s79, 15
	s_nop 0
	v_writelane_b32 v253, s80, 16
	s_nop 0
	v_writelane_b32 v253, s81, 17
	s_nop 0
	v_writelane_b32 v253, s82, 18
	s_nop 0
	v_writelane_b32 v253, s83, 19
	s_nop 0
	v_writelane_b32 v253, s84, 20
	s_nop 0
	v_writelane_b32 v253, s85, 21
	s_nop 0
	v_writelane_b32 v253, s86, 22
	s_nop 0
	v_writelane_b32 v253, s87, 23
	s_nop 0
	v_writelane_b32 v253, s88, 24
	s_nop 0
	v_writelane_b32 v253, s89, 25
	s_nop 0
	v_writelane_b32 v253, s90, 26
	s_nop 0
	v_writelane_b32 v253, s91, 27
	s_nop 0
	v_writelane_b32 v253, s92, 28
	s_nop 0
	v_writelane_b32 v253, s93, 29
	s_nop 0
	v_writelane_b32 v253, s94, 30
	s_nop 0
	v_writelane_b32 v253, s95, 31
	s_nop 0
	v_writelane_b32 v253, s96, 32
	s_nop 0
	v_writelane_b32 v253, s97, 33
	s_nop 0
	v_writelane_b32 v253, vcc_lo, 34
	s_nop 0
	v_writelane_b32 v253, vcc_hi, 35
	s_nop 1
	v_readlane_b32 s84, v254, 35
	s_nop 3
	v_readlane_b32 s98, v254, 38
	s_nop 3
	s_cmp_gt_u32 s98, 2
	s_cbranch_scc1 .Lcvrs_p30
; #define LAS __attribute__((address_space(3)))
; __global__ void __launch_bounds__(NWAVES * 64, 2) mk_fwd(Args args) {
;     ...
;             PH_LOCALS
;             LAS float* scr = (LAS float*)(lds + RING_OFF + wave * 16640);   static_assert(8 * 16640 <= LDSCTL_OFF, "converter scratch below the LDS control words");
;             constexpr int I_UP = (D / 64) * (NUP / 64), I_DN = (DFF / 64) * (D / 64), I_IN = (D / 64) * (DINP / 64), I_GLU = 16 * 16, I_L = 4 * 16, I_V1 = 16 * 4, I_V2 = 4 * 16,
;                           I_BS5 = 16 * 32, I_BAT = 8 * 32, I_BRW = 16 * 32, I_OUT = 32 * 32;
;             constexpr int NITEMS = 2 * I_UP + 2 * I_DN + I_IN + I_GLU + 3 * I_L + I_V1 + I_V2 + I_BS5 + I_BAT + I_BRW + I_OUT;
;             const int lv = l > 0 ? l - 1 : 0;
;     ...
;             for (int it = gw; it < NITEMS; it += NGW) {
;                 ConvItem ca; CONV_DESC(ca, it);
;                 float va[64];
;                 conv_load(ca, lane, va);
;                 conv_store(ca, scr, lane, va);
;             }
	v_readlane_b32 s0, v254, 8
	v_readlane_b32 s4, v254, 10
	v_readlane_b32 s1, v254, 9
	v_mbcnt_lo_u32_b32 v11, -1, 0
	v_mbcnt_hi_u32_b32 v11, -1, v11
	s_load_dword s6, s[0:1], 0x0
	s_mov_b32 s3, s84
	s_waitcnt lgkmcnt(0)
	s_movk_i32 s6, 64
	s_cmp_gt_u32 s4, 3
	s_cbranch_scc1 .Lcvp30_ret
	s_lshl_b32 s3, s3, 2
	v_readlane_b32 s0, v254, 0
	s_add_i32 s3, s3, s4
	s_add_i32 s3, s3, 0x4700
	v_readlane_b32 s1, v254, 1
	s_cmpk_gt_i32 s3, 21439
	s_cbranch_scc1 .Lcvp30_ret
	s_load_dwordx2 s[8:9], s[0:1], 0x138
	v_readlane_b32 s14, v254, 38
	s_nop 0
	s_add_i32 s14, s14, 1
	s_mulk_i32 s4, 0x4100
	s_add_i32 s7, s4, 0
	v_sub_u32_e64 v0, s14, 1 clamp
	s_lshl_b32 s33, s6, 3
	v_readfirstlane_b32 s4, v0
	s_lshl_b32 s96, s4, 16
	s_waitcnt lgkmcnt(0)
	s_add_u32 s4, s8, 0x22800000
	s_addc_u32 s5, s9, 0
	v_writelane_b32 v254, s4, 39
	s_mov_b32 s15, s97
	v_and_b32_e32 v0, 7, v11
	v_writelane_b32 v254, s5, 40
	s_add_u32 s4, s8, 0x22780000
	s_addc_u32 s5, s9, 0
	v_writelane_b32 v254, s4, 41
	v_ashrrev_i32_e32 v13, 3, v11
	v_lshlrev_b32_e32 v10, 3, v0
	v_writelane_b32 v254, s5, 42
	s_lshl_b32 s4, s14, 18
	s_add_u32 s10, s8, 0x22700000
	s_addc_u32 s11, s9, 0
	v_writelane_b32 v254, s10, 43
	s_mov_b32 s5, s97
	v_mul_u32_u24_e32 v0, 0x820, v0
	v_writelane_b32 v254, s11, 44
	s_mul_i32 s10, s14, 0x18000
	s_mov_b32 s11, s97
	v_writelane_b32 v254, s10, 45
	v_lshlrev_b32_e32 v1, 2, v13
	v_lshl_add_u32 v12, v11, 2, s7
	v_writelane_b32 v254, s11, 46
	s_add_u32 s10, s8, 0x22680000
	s_addc_u32 s11, s9, 0
	v_writelane_b32 v254, s10, 47
	v_add3_u32 v14, s7, v0, v1
	s_mov_b32 s41, s97
	v_writelane_b32 v254, s11, 48
	s_add_u32 s10, s8, 0x22600000
	s_addc_u32 s11, s9, 0
	v_writelane_b32 v254, s10, 49
	s_nop 1
	v_writelane_b32 v254, s11, 50
	s_lshl_b32 s10, s14, 20
	s_mov_b32 s11, s97
	v_writelane_b32 v254, s10, 51
	s_nop 1
	v_writelane_b32 v254, s11, 52
	s_add_u32 s10, s8, 0x22400000
	s_addc_u32 s11, s9, 0
	v_writelane_b32 v254, s10, 53
	s_nop 1
	v_writelane_b32 v254, s11, 54
	s_lshl_b32 s10, s14, 21
	s_mov_b32 s11, s97
	v_writelane_b32 v254, s10, 55
	s_nop 1
	v_writelane_b32 v254, s11, 56
	s_add_u32 s10, s8, 0x22e80000
	s_addc_u32 s11, s9, 0
	v_writelane_b32 v254, s10, 57
	s_nop 1
	v_writelane_b32 v254, s11, 58
	s_add_u32 s10, s8, 0x27b80000
	s_addc_u32 s11, s9, 0
	v_writelane_b32 v254, s10, 59
	s_nop 1
	v_writelane_b32 v254, s11, 60
	s_add_u32 s10, s8, 0x22880000
	s_addc_u32 s11, s9, 0
	v_writelane_b32 v254, s10, 61
	s_nop 1
	v_writelane_b32 v254, s11, 62
	s_lshl_b32 s10, s14, 22
	s_add_u32 s12, s8, 0x23280000
	s_addc_u32 s13, s9, 0
	v_writelane_b32 v254, s12, 63
	s_mov_b32 s11, s97
	s_nop 0
	v_writelane_b32 v255, s13, 0
	s_mul_i32 s12, s14, 0xac0000
	s_mov_b32 s13, s97
	v_writelane_b32 v255, s12, 1
	s_nop 1
	v_writelane_b32 v255, s13, 2
	s_add_u32 s12, s8, 0x26580000
	s_addc_u32 s13, s9, 0
	v_writelane_b32 v255, s12, 3
	s_nop 1
	v_writelane_b32 v255, s13, 4
	s_add_u32 s12, s8, 0x1d200000
	s_addc_u32 s13, s9, 0
	s_lshl_b32 s40, s14, 11
	v_writelane_b32 v255, s12, 5
	s_add_u32 s16, s8, 0x1e800000
	s_addc_u32 s17, s9, 0
	v_writelane_b32 v255, s13, 6
	v_writelane_b32 v255, s16, 7
	s_mul_i32 s12, s14, 0x1de0000
	s_mul_i32 s14, s14, 0x1580000
	v_writelane_b32 v255, s17, 8
	v_writelane_b32 v255, s14, 9
	s_mov_b32 s13, s97
	s_nop 0
	v_writelane_b32 v255, s15, 10
	s_add_u32 s14, s8, 0x23a80000
	s_addc_u32 s15, s9, 0
	v_writelane_b32 v255, s14, 11
	s_add_u32 s8, s8, 0x1a700000
	s_addc_u32 s9, s9, 0
	v_writelane_b32 v255, s15, 12
	v_writelane_b32 v255, s8, 13
	s_lshl_b64 s[4:5], s[4:5], 2
	s_lshl_b32 s7, s3, 4
	v_writelane_b32 v255, s9, 14
	v_writelane_b32 v255, s4, 15
	s_add_i32 s72, s7, 0xc00
	s_lshl_b32 s7, s3, 1
	v_writelane_b32 v255, s5, 16
	s_lshl_b64 s[4:5], s[10:11], 2
	v_writelane_b32 v255, s4, 17
	s_lshl_b32 s66, s3, 6
	s_lshl_b32 s67, s6, 9
	v_writelane_b32 v255, s5, 18
	s_lshl_b64 s[4:5], s[12:13], 2
	v_writelane_b32 v255, s4, 19
	s_lshl_b32 s68, s3, 5
	s_lshl_b32 s69, s6, 8
	v_writelane_b32 v255, s5, 20
	v_writelane_b32 v255, s80, 21
	s_lshl_b32 s70, s3, 2
	s_lshl_b32 s71, s6, 5
	v_writelane_b32 v255, s81, 22
	v_writelane_b32 v255, s82, 23
	s_lshl_b32 s73, s6, 7
	s_add_i32 s74, s7, 0x13500
	s_lshl_b32 s75, s6, 4
	v_writelane_b32 v255, s83, 24
	s_branch .Lcvp30_31

; #define LAS __attribute__((address_space(3)))
; __global__ void __launch_bounds__(NWAVES * 64, 2) mk_fwd(Args args) {
;     ...
;             PH_LOCALS
;             LAS float* scr = (LAS float*)(lds + RING_OFF + wave * 16640);   static_assert(8 * 16640 <= LDSCTL_OFF, "converter scratch below the LDS control words");
;             constexpr int I_UP = (D / 64) * (NUP / 64), I_DN = (DFF / 64) * (D / 64), I_IN = (D / 64) * (DINP / 64), I_GLU = 16 * 16, I_L = 4 * 16, I_V1 = 16 * 4, I_V2 = 4 * 16,
;                           I_BS5 = 16 * 32, I_BAT = 8 * 32, I_BRW = 16 * 32, I_OUT = 32 * 32;
;             constexpr int NITEMS = 2 * I_UP + 2 * I_DN + I_IN + I_GLU + 3 * I_L + I_V1 + I_V2 + I_BS5 + I_BAT + I_BRW + I_OUT;
;             const int lv = l > 0 ? l - 1 : 0;
;     ...
;             for (int it = gw; it < NITEMS; it += NGW) {
;                 ConvItem ca; CONV_DESC(ca, it);
;                 float va[64];
;                 conv_load(ca, lane, va);
;                 conv_store(ca, scr, lane, va);
;             }
.Lcvp30_ret:
.Lcvrs_p30:
	v_readlane_b32 s0, v254, 8
	v_readlane_b32 s4, v254, 10
	v_readlane_b32 s1, v254, 9
	v_mbcnt_lo_u32_b32 v11, -1, 0
	v_mbcnt_hi_u32_b32 v11, -1, v11
	s_load_dword s6, s[0:1], 0x0
	s_mov_b32 s3, s84
	s_waitcnt lgkmcnt(0)
	s_movk_i32 s6, 64
	s_cmp_gt_u32 s4, 3
	s_cbranch_scc1 .Lcvp31_ret
	s_lshl_b32 s3, s3, 2
	v_readlane_b32 s0, v254, 0
	s_add_i32 s3, s3, s4
	s_add_i32 s3, s3, 0x51c0
	v_readlane_b32 s1, v254, 1
	s_cmpk_gt_i32 s3, 25215
	s_cbranch_scc1 .Lcvp31_ret
	s_load_dwordx2 s[8:9], s[0:1], 0x138
	v_readlane_b32 s14, v254, 38
	s_mulk_i32 s4, 0x4100
	s_add_i32 s7, s4, 0
	v_sub_u32_e64 v0, s14, 1 clamp
	s_lshl_b32 s33, s6, 3
	v_readfirstlane_b32 s4, v0
	s_lshl_b32 s96, s4, 16
	s_waitcnt lgkmcnt(0)
	s_add_u32 s4, s8, 0x22800000
	s_addc_u32 s5, s9, 0
	v_writelane_b32 v254, s4, 39
	s_mov_b32 s15, s97
	v_and_b32_e32 v0, 7, v11
	v_writelane_b32 v254, s5, 40
	s_add_u32 s4, s8, 0x22780000
	s_addc_u32 s5, s9, 0
	v_writelane_b32 v254, s4, 41
	v_ashrrev_i32_e32 v13, 3, v11
	v_lshlrev_b32_e32 v10, 3, v0
	v_writelane_b32 v254, s5, 42
	s_lshl_b32 s4, s14, 18
	s_add_u32 s10, s8, 0x22700000
	s_addc_u32 s11, s9, 0
	v_writelane_b32 v254, s10, 43
	s_mov_b32 s5, s97
	v_mul_u32_u24_e32 v0, 0x820, v0
	v_writelane_b32 v254, s11, 44
	s_mul_i32 s10, s14, 0x18000
	s_mov_b32 s11, s97
	v_writelane_b32 v254, s10, 45
	v_lshlrev_b32_e32 v1, 2, v13
	v_lshl_add_u32 v12, v11, 2, s7
	v_writelane_b32 v254, s11, 46
	s_add_u32 s10, s8, 0x22680000
	s_addc_u32 s11, s9, 0
	v_writelane_b32 v254, s10, 47
	v_add3_u32 v14, s7, v0, v1
	s_mov_b32 s41, s97
	v_writelane_b32 v254, s11, 48
	s_add_u32 s10, s8, 0x22600000
	s_addc_u32 s11, s9, 0
	v_writelane_b32 v254, s10, 49
	s_nop 1
	v_writelane_b32 v254, s11, 50
	s_lshl_b32 s10, s14, 20
	s_mov_b32 s11, s97
	v_writelane_b32 v254, s10, 51
	s_nop 1
	v_writelane_b32 v254, s11, 52
	s_add_u32 s10, s8, 0x22400000
	s_addc_u32 s11, s9, 0
	v_writelane_b32 v254, s10, 53
	s_nop 1
	v_writelane_b32 v254, s11, 54
	s_lshl_b32 s10, s14, 21
	s_mov_b32 s11, s97
	v_writelane_b32 v254, s10, 55
	s_nop 1
	v_writelane_b32 v254, s11, 56
	s_add_u32 s10, s8, 0x22e80000
	s_addc_u32 s11, s9, 0
	v_writelane_b32 v254, s10, 57
	s_nop 1
	v_writelane_b32 v254, s11, 58
	s_add_u32 s10, s8, 0x27b80000
	s_addc_u32 s11, s9, 0
	v_writelane_b32 v254, s10, 59
	s_nop 1
	v_writelane_b32 v254, s11, 60
	s_add_u32 s10, s8, 0x22880000
	s_addc_u32 s11, s9, 0
	v_writelane_b32 v254, s10, 61
	s_nop 1
	v_writelane_b32 v254, s11, 62
	s_lshl_b32 s10, s14, 22
	s_add_u32 s12, s8, 0x23280000
	s_addc_u32 s13, s9, 0
	v_writelane_b32 v254, s12, 63
	s_mov_b32 s11, s97
	s_nop 0
	v_writelane_b32 v255, s13, 0
	s_mul_i32 s12, s14, 0xac0000
	s_mov_b32 s13, s97
	v_writelane_b32 v255, s12, 1
	s_nop 1
	v_writelane_b32 v255, s13, 2
	s_add_u32 s12, s8, 0x26580000
	s_addc_u32 s13, s9, 0
	v_writelane_b32 v255, s12, 3
	s_nop 1
	v_writelane_b32 v255, s13, 4
	s_add_u32 s12, s8, 0x1d200000
	s_addc_u32 s13, s9, 0
	s_lshl_b32 s40, s14, 11
	v_writelane_b32 v255, s12, 5
	s_add_u32 s16, s8, 0x1e800000
	s_addc_u32 s17, s9, 0
	v_writelane_b32 v255, s13, 6
	v_writelane_b32 v255, s16, 7
	s_mul_i32 s12, s14, 0x1de0000
	s_mul_i32 s14, s14, 0x1580000
	v_writelane_b32 v255, s17, 8
	v_writelane_b32 v255, s14, 9
	s_mov_b32 s13, s97
	s_nop 0
	v_writelane_b32 v255, s15, 10
	s_add_u32 s14, s8, 0x23a80000
	s_addc_u32 s15, s9, 0
	v_writelane_b32 v255, s14, 11
	s_add_u32 s8, s8, 0x1a700000
	s_addc_u32 s9, s9, 0
	v_writelane_b32 v255, s15, 12
	v_writelane_b32 v255, s8, 13
	s_lshl_b64 s[4:5], s[4:5], 2
	s_lshl_b32 s7, s3, 4
	v_writelane_b32 v255, s9, 14
	v_writelane_b32 v255, s4, 15
	s_add_i32 s72, s7, 0xc00
	s_lshl_b32 s7, s3, 1
	v_writelane_b32 v255, s5, 16
	s_lshl_b64 s[4:5], s[10:11], 2
	v_writelane_b32 v255, s4, 17
	s_lshl_b32 s66, s3, 6
	s_lshl_b32 s67, s6, 9
	v_writelane_b32 v255, s5, 18
	s_lshl_b64 s[4:5], s[12:13], 2
	v_writelane_b32 v255, s4, 19
	s_lshl_b32 s68, s3, 5
	s_lshl_b32 s69, s6, 8
	v_writelane_b32 v255, s5, 20
	v_writelane_b32 v255, s80, 21
	s_lshl_b32 s70, s3, 2
	s_lshl_b32 s71, s6, 5
	v_writelane_b32 v255, s81, 22
	v_writelane_b32 v255, s82, 23
	s_lshl_b32 s73, s6, 7
	s_add_i32 s74, s7, 0x13500
	s_lshl_b32 s75, s6, 4
	v_writelane_b32 v255, s83, 24
	s_branch .Lcvp31_31

; #define LAS __attribute__((address_space(3)))
; #define IN(k) in_range(lo, hi, (k))
; __global__ void __launch_bounds__(NWAVES * 64, 2) mk_fwd(Args args) {
;     ...
;         if (EN(0) && IN(pb + 0)) {
;             PH_LOCALS
;             LAS float* scr = (LAS float*)(lds + RING_OFF + wave * 16640);   static_assert(8 * 16640 <= LDSCTL_OFF, "converter scratch below the LDS control words");
;             constexpr int I_UP = (D / 64) * (NUP / 64), I_DN = (DFF / 64) * (D / 64), I_IN = (D / 64) * (DINP / 64), I_GLU = 16 * 16, I_L = 4 * 16, I_V1 = 16 * 4, I_V2 = 4 * 16,
;                           I_BS5 = 16 * 32, I_BAT = 8 * 32, I_BRW = 16 * 32, I_OUT = 32 * 32;
;             constexpr int NITEMS = 2 * I_UP + 2 * I_DN + I_IN + I_GLU + 3 * I_L + I_V1 + I_V2 + I_BS5 + I_BAT + I_BRW + I_OUT;
;             const int lv = l > 0 ? l - 1 : 0;
.LBB0_1151:
	v_readlane_b32 s99, v254, 35
	v_readlane_b32 s98, v254, 38
	s_nop 3
	s_cmp_lt_u32 s99, 96
	s_cbranch_scc1 .Lcvskip_p13
	s_cmp_gt_u32 s98, 2
	s_cbranch_scc1 .Lcvskip_p13
	v_mov_b32_e32 v250, v254
	v_mov_b32_e32 v251, v255
	v_writelane_b32 v252, s0, 0
	s_nop 0
	v_writelane_b32 v252, s1, 1
	s_nop 0
	v_writelane_b32 v252, s2, 2
	s_nop 0
	v_writelane_b32 v252, s3, 3
	s_nop 0
	v_writelane_b32 v252, s4, 4
	s_nop 0
	v_writelane_b32 v252, s5, 5
	s_nop 0
	v_writelane_b32 v252, s6, 6
	s_nop 0
	v_writelane_b32 v252, s7, 7
	s_nop 0
	v_writelane_b32 v252, s8, 8
	s_nop 0
	v_writelane_b32 v252, s9, 9
	s_nop 0
	v_writelane_b32 v252, s10, 10
	s_nop 0
	v_writelane_b32 v252, s11, 11
	s_nop 0
	v_writelane_b32 v252, s12, 12
	s_nop 0
	v_writelane_b32 v252, s13, 13
	s_nop 0
	v_writelane_b32 v252, s14, 14
	s_nop 0
	v_writelane_b32 v252, s15, 15
	s_nop 0
	v_writelane_b32 v252, s16, 16
	s_nop 0
	v_writelane_b32 v252, s17, 17
	s_nop 0
	v_writelane_b32 v252, s18, 18
	s_nop 0
	v_writelane_b32 v252, s19, 19
	s_nop 0
	v_writelane_b32 v252, s20, 20
	s_nop 0
	v_writelane_b32 v252, s21, 21
	s_nop 0
	v_writelane_b32 v252, s22, 22
	s_nop 0
	v_writelane_b32 v252, s23, 23
	s_nop 0
	v_writelane_b32 v252, s24, 24
	s_nop 0
	v_writelane_b32 v252, s25, 25
	s_nop 0
	v_writelane_b32 v252, s26, 26
	s_nop 0
	v_writelane_b32 v252, s27, 27
	s_nop 0
	v_writelane_b32 v252, s28, 28
	s_nop 0
	v_writelane_b32 v252, s29, 29
	s_nop 0
	v_writelane_b32 v252, s30, 30
	s_nop 0
	v_writelane_b32 v252, s31, 31
	s_nop 0
	v_writelane_b32 v252, s32, 32
	s_nop 0
	v_writelane_b32 v252, s33, 33
	s_nop 0
	v_writelane_b32 v252, s34, 34
	s_nop 0
	v_writelane_b32 v252, s35, 35
	s_nop 0
	v_writelane_b32 v252, s36, 36
	s_nop 0
	v_writelane_b32 v252, s37, 37
	s_nop 0
	v_writelane_b32 v252, s38, 38
	s_nop 0
	v_writelane_b32 v252, s39, 39
	s_nop 0
	v_writelane_b32 v252, s40, 40
	s_nop 0
	v_writelane_b32 v252, s41, 41
	s_nop 0
	v_writelane_b32 v252, s42, 42
	s_nop 0
	v_writelane_b32 v252, s43, 43
	s_nop 0
	v_writelane_b32 v252, s44, 44
	s_nop 0
	v_writelane_b32 v252, s45, 45
	s_nop 0
	v_writelane_b32 v252, s46, 46
	s_nop 0
	v_writelane_b32 v252, s47, 47
	s_nop 0
	v_writelane_b32 v252, s48, 48
	s_nop 0
	v_writelane_b32 v252, s49, 49
	s_nop 0
	v_writelane_b32 v252, s50, 50
	s_nop 0
	v_writelane_b32 v252, s51, 51
	s_nop 0
	v_writelane_b32 v252, s52, 52
	s_nop 0
	v_writelane_b32 v252, s53, 53
	s_nop 0
	v_writelane_b32 v252, s54, 54
	s_nop 0
	v_writelane_b32 v252, s55, 55
	s_nop 0
	v_writelane_b32 v252, s56, 56
	s_nop 0
	v_writelane_b32 v252, s57, 57
	s_nop 0
	v_writelane_b32 v252, s58, 58
	s_nop 0
	v_writelane_b32 v252, s59, 59
	s_nop 0
	v_writelane_b32 v252, s60, 60
	s_nop 0
	v_writelane_b32 v252, s61, 61
	s_nop 0
	v_writelane_b32 v252, s62, 62
	s_nop 0
	v_writelane_b32 v252, s63, 63
	s_nop 0
	v_writelane_b32 v253, s64, 0
	s_nop 0
	v_writelane_b32 v253, s65, 1
	s_nop 0
	v_writelane_b32 v253, s66, 2
	s_nop 0
	v_writelane_b32 v253, s67, 3
	s_nop 0
	v_writelane_b32 v253, s68, 4
	s_nop 0
	v_writelane_b32 v253, s69, 5
	s_nop 0
	v_writelane_b32 v253, s70, 6
	s_nop 0
	v_writelane_b32 v253, s71, 7
	s_nop 0
	v_writelane_b32 v253, s72, 8
	s_nop 0
	v_writelane_b32 v253, s73, 9
	s_nop 0
	v_writelane_b32 v253, s74, 10
	s_nop 0
	v_writelane_b32 v253, s75, 11
	s_nop 0
	v_writelane_b32 v253, s76, 12
	s_nop 0
	v_writelane_b32 v253, s77, 13
	s_nop 0
	v_writelane_b32 v253, s78, 14
	s_nop 0
	v_writelane_b32 v253, s79, 15
	s_nop 0
	v_writelane_b32 v253, s80, 16
	s_nop 0
	v_writelane_b32 v253, s81, 17
	s_nop 0
	v_writelane_b32 v253, s82, 18
	s_nop 0
	v_writelane_b32 v253, s83, 19
	s_nop 0
	v_writelane_b32 v253, s84, 20
	s_nop 0
	v_writelane_b32 v253, s85, 21
	s_nop 0
	v_writelane_b32 v253, s86, 22
	s_nop 0
	v_writelane_b32 v253, s87, 23
	s_nop 0
	v_writelane_b32 v253, s88, 24
	s_nop 0
	v_writelane_b32 v253, s89, 25
	s_nop 0
	v_writelane_b32 v253, s90, 26
	s_nop 0
	v_writelane_b32 v253, s91, 27
	s_nop 0
	v_writelane_b32 v253, s92, 28
	s_nop 0
	v_writelane_b32 v253, s93, 29
	s_nop 0
	v_writelane_b32 v253, s94, 30
	s_nop 0
	v_writelane_b32 v253, s95, 31
	s_nop 0
	v_writelane_b32 v253, s96, 32
	s_nop 0
	v_writelane_b32 v253, s97, 33
	s_nop 0
	v_writelane_b32 v253, vcc_lo, 34
	s_nop 0
	v_writelane_b32 v253, vcc_hi, 35
	s_nop 1
	v_readlane_b32 s84, v254, 35
	s_nop 3
	v_readlane_b32 s0, v254, 8
	v_readlane_b32 s4, v254, 10
	v_readlane_b32 s1, v254, 9
	v_mbcnt_lo_u32_b32 v11, -1, 0
	v_mbcnt_hi_u32_b32 v11, -1, v11
	s_load_dword s6, s[0:1], 0x0
	s_mov_b32 s3, s84
	s_waitcnt lgkmcnt(0)
	s_movk_i32 s6, 80
	s_cmp_gt_u32 s4, 3
	s_cbranch_scc1 .Lcvp130_ret
; #define LAS __attribute__((address_space(3)))
; __global__ void __launch_bounds__(NWAVES * 64, 2) mk_fwd(Args args) {
;     ...
;             PH_LOCALS
;             LAS float* scr = (LAS float*)(lds + RING_OFF + wave * 16640);   static_assert(8 * 16640 <= LDSCTL_OFF, "converter scratch below the LDS control words");
;             constexpr int I_UP = (D / 64) * (NUP / 64), I_DN = (DFF / 64) * (D / 64), I_IN = (D / 64) * (DINP / 64), I_GLU = 16 * 16, I_L = 4 * 16, I_V1 = 16 * 4, I_V2 = 4 * 16,
;                           I_BS5 = 16 * 32, I_BAT = 8 * 32, I_BRW = 16 * 32, I_OUT = 32 * 32;
;             constexpr int NITEMS = 2 * I_UP + 2 * I_DN + I_IN + I_GLU + 3 * I_L + I_V1 + I_V2 + I_BS5 + I_BAT + I_BRW + I_OUT;
;             const int lv = l > 0 ? l - 1 : 0;
;     ...
;             for (int it = gw; it < NITEMS; it += NGW) {
;                 ConvItem ca; CONV_DESC(ca, it);
;                 float va[64];
;                 conv_load(ca, lane, va);
;                 conv_store(ca, scr, lane, va);
;             }
	s_lshl_b32 s3, s3, 2
	v_readlane_b32 s0, v254, 0
	s_add_i32 s3, s3, s4
	s_add_i32 s3, s3, 0x2980
	v_readlane_b32 s1, v254, 1
	s_cmpk_gt_i32 s3, 18687
	s_cbranch_scc1 .Lcvp130_ret
	s_load_dwordx2 s[8:9], s[0:1], 0x138
	v_readlane_b32 s14, v254, 38
	s_nop 0
	s_add_i32 s14, s14, 1
	s_mulk_i32 s4, 0x4100
	s_add_i32 s7, s4, 0
	v_sub_u32_e64 v0, s14, 1 clamp
	s_lshl_b32 s33, s6, 3
	v_readfirstlane_b32 s4, v0
	s_lshl_b32 s96, s4, 16
	s_waitcnt lgkmcnt(0)
	s_add_u32 s4, s8, 0x22800000
	s_addc_u32 s5, s9, 0
	v_writelane_b32 v254, s4, 39
	s_mov_b32 s15, s97
	v_and_b32_e32 v0, 7, v11
	v_writelane_b32 v254, s5, 40
	s_add_u32 s4, s8, 0x22780000
	s_addc_u32 s5, s9, 0
	v_writelane_b32 v254, s4, 41
	v_ashrrev_i32_e32 v13, 3, v11
	v_lshlrev_b32_e32 v10, 3, v0
	v_writelane_b32 v254, s5, 42
	s_lshl_b32 s4, s14, 18
	s_add_u32 s10, s8, 0x22700000
	s_addc_u32 s11, s9, 0
	v_writelane_b32 v254, s10, 43
	s_mov_b32 s5, s97
	v_mul_u32_u24_e32 v0, 0x820, v0
	v_writelane_b32 v254, s11, 44
	s_mul_i32 s10, s14, 0x18000
	s_mov_b32 s11, s97
	v_writelane_b32 v254, s10, 45
	v_lshlrev_b32_e32 v1, 2, v13
	v_lshl_add_u32 v12, v11, 2, s7
	v_writelane_b32 v254, s11, 46
	s_add_u32 s10, s8, 0x22680000
	s_addc_u32 s11, s9, 0
	v_writelane_b32 v254, s10, 47
	v_add3_u32 v14, s7, v0, v1
	s_mov_b32 s41, s97
	v_writelane_b32 v254, s11, 48
	s_add_u32 s10, s8, 0x22600000
	s_addc_u32 s11, s9, 0
	v_writelane_b32 v254, s10, 49
	s_nop 1
	v_writelane_b32 v254, s11, 50
	s_lshl_b32 s10, s14, 20
	s_mov_b32 s11, s97
	v_writelane_b32 v254, s10, 51
	s_nop 1
	v_writelane_b32 v254, s11, 52
	s_add_u32 s10, s8, 0x22400000
	s_addc_u32 s11, s9, 0
	v_writelane_b32 v254, s10, 53
	s_nop 1
	v_writelane_b32 v254, s11, 54
	s_lshl_b32 s10, s14, 21
	s_mov_b32 s11, s97
	v_writelane_b32 v254, s10, 55
	s_nop 1
	v_writelane_b32 v254, s11, 56
	s_add_u32 s10, s8, 0x22e80000
	s_addc_u32 s11, s9, 0
	v_writelane_b32 v254, s10, 57
	s_nop 1
	v_writelane_b32 v254, s11, 58
	s_add_u32 s10, s8, 0x27b80000
	s_addc_u32 s11, s9, 0
	v_writelane_b32 v254, s10, 59
	s_nop 1
	v_writelane_b32 v254, s11, 60
	s_add_u32 s10, s8, 0x22880000
	s_addc_u32 s11, s9, 0
	v_writelane_b32 v254, s10, 61
	s_nop 1
	v_writelane_b32 v254, s11, 62
	s_lshl_b32 s10, s14, 22
	s_add_u32 s12, s8, 0x23280000
	s_addc_u32 s13, s9, 0
	v_writelane_b32 v254, s12, 63
	s_mov_b32 s11, s97
	s_nop 0
	v_writelane_b32 v255, s13, 0
	s_mul_i32 s12, s14, 0xac0000
	s_mov_b32 s13, s97
	v_writelane_b32 v255, s12, 1
	s_nop 1
	v_writelane_b32 v255, s13, 2
	s_add_u32 s12, s8, 0x26580000
	s_addc_u32 s13, s9, 0
	v_writelane_b32 v255, s12, 3
	s_nop 1
	v_writelane_b32 v255, s13, 4
	s_add_u32 s12, s8, 0x1d200000
	s_addc_u32 s13, s9, 0
	s_lshl_b32 s40, s14, 11
	v_writelane_b32 v255, s12, 5
	s_add_u32 s16, s8, 0x1e800000
	s_addc_u32 s17, s9, 0
	v_writelane_b32 v255, s13, 6
	v_writelane_b32 v255, s16, 7
	s_mul_i32 s12, s14, 0x1de0000
	s_mul_i32 s14, s14, 0x1580000
	v_writelane_b32 v255, s17, 8
	v_writelane_b32 v255, s14, 9
	s_mov_b32 s13, s97
	s_nop 0
	v_writelane_b32 v255, s15, 10
	s_add_u32 s14, s8, 0x23a80000
	s_addc_u32 s15, s9, 0
	v_writelane_b32 v255, s14, 11
	s_add_u32 s8, s8, 0x1a700000
	s_addc_u32 s9, s9, 0
	v_writelane_b32 v255, s15, 12
	v_writelane_b32 v255, s8, 13
	s_lshl_b64 s[4:5], s[4:5], 2
	s_lshl_b32 s7, s3, 4
	v_writelane_b32 v255, s9, 14
	v_writelane_b32 v255, s4, 15
	s_add_i32 s72, s7, 0xc00
	s_lshl_b32 s7, s3, 1
	v_writelane_b32 v255, s5, 16
	s_lshl_b64 s[4:5], s[10:11], 2
	v_writelane_b32 v255, s4, 17
	s_lshl_b32 s66, s3, 6
	s_lshl_b32 s67, s6, 9
	v_writelane_b32 v255, s5, 18
	s_lshl_b64 s[4:5], s[12:13], 2
	v_writelane_b32 v255, s4, 19
	s_lshl_b32 s68, s3, 5
	s_lshl_b32 s69, s6, 8
	v_writelane_b32 v255, s5, 20
	v_writelane_b32 v255, s80, 21
	s_lshl_b32 s70, s3, 2
	s_lshl_b32 s71, s6, 5
	v_writelane_b32 v255, s81, 22
	v_writelane_b32 v255, s82, 23
	s_lshl_b32 s73, s6, 7
	s_add_i32 s74, s7, 0x13500
	s_lshl_b32 s75, s6, 4
	v_writelane_b32 v255, s83, 24
	s_branch .Lcvp130_31
